# sel tile: four exps (instead of two) between the rescale compare and its branch
# baseline (speedup 1.0000x reference)
; __device__ __forceinline__ unsigned pk4_fp8(float a, float b, float c, float d) { unsigned w = 0u; w = __builtin_amdgcn_cvt_pk_fp8_f32(a, b, w, false); w = __builtin_amdgcn_cvt_pk_fp8_f32(c, d, w, true); return w; }
; __device__ __forceinline__ float xmax16(float v) { float a = v, b = v; PL_SWAP16(a, b); return fmaxf(a, b); }
; __device__ __forceinline__ float xmax32(float v) { float a = v, b = v; PL_SWAP32(a, b); return fmaxf(a, b); }
; #define LGKM_W(n) asm volatile("s_waitcnt lgkmcnt(" #n ")" ::: "memory"); SBAR()
; #define PV8_MM(dt) do { g.o[dt] = __builtin_amdgcn_mfma_f32_16x16x32_fp8_fp8(f.a[dt][0], b0, g.o[dt], 0, 0, 0); g.o[dt] = __builtin_amdgcn_mfma_f32_16x16x32_fp8_fp8(f.a[dt][1], b1, g.o[dt], 0, 0, 0); } while (0)
; template <class G> __device__ __forceinline__ void pv8_mm(G& g, const f32x4 (&s)[4], const VT8Frag& f) {
;     ...
;     unsigned pa[4];
; #pragma unroll
;     for (int T_ = 0; T_ < 4; ++T_) pa[T_] = pk4_fp8(s[T_][0], s[T_][1], s[T_][2], s[T_][3]);
;     const long b0 = (long)(((unsigned long long)pa[1] << 32) | pa[0]), b1 = (long)(((unsigned long long)pa[3] << 32) | pa[2]);
;     LGKM_W(14); PV8_MM(0); LGKM_W(12); PV8_MM(1); LGKM_W(10); PV8_MM(2); LGKM_W(8); PV8_MM(3);
;     LGKM_W(6); PV8_MM(4); LGKM_W(4); PV8_MM(5); LGKM_W(2); PV8_MM(6); LGKM_W(0); PV8_MM(7);
; template <class G> __device__ __forceinline__ void online_sm8(f32x4 (&s)[4], G& g, const float ref) {
;     float mx = s[0][0];
; #pragma unroll
;     for (int T_ = 0; T_ < 4; ++T_)
; #pragma unroll
;         for (int i = 0; i < 4; ++i) mx = fmaxf(mx, s[T_][i]);
;     const float t = mx + (ref - 5.f);
;     if (!__all(t <= g.m + SM_THR8)) {
;         const float mr = xmax32(xmax16(t));
;         const float mn = fmaxf(g.m, mr); const float al = __builtin_amdgcn_exp2f(g.m - mn); g.m = mn; g.l *= al;
; #pragma unroll
;         for (int dt = 0; dt < 8; ++dt) g.o[dt] = g.o[dt] * al;
;         const float d = ref - mn;
; #pragma unroll
;         for (int T_ = 0; T_ < 4; ++T_)
; #pragma unroll
;             for (int i = 0; i < 4; ++i) s[T_][i] += d;
;     }
;     float ps = 0.f;
; #pragma unroll
;     for (int T_ = 0; T_ < 4; ++T_)
; #pragma unroll
;         for (int i = 0; i < 4; ++i) { s[T_][i] = __builtin_amdgcn_exp2f(s[T_][i]); ps += s[T_][i]; }
;     g.l += ps;
.LBB0_1806:
	v_max_f32_e32 v18, v84, v85
	v_max3_f32 v18, v18, v86, v87
	v_max3_f32 v18, v18, v88, v89
	v_max3_f32 v18, v18, v90, v91
	v_max3_f32 v18, v18, v92, v93
	v_max3_f32 v18, v18, v94, v95
	v_max3_f32 v18, v18, v96, v97
	v_max3_f32 v114, v18, v98, v99
	v_cmp_nle_f32_e32 vcc, v114, v226
	v_exp_f32_e32 v240, v84
	v_exp_f32_e32 v241, v85
	v_exp_f32_e32 v242, v86
	v_exp_f32_e32 v243, v87
	s_cbranch_vccnz .Lsel_resc_g0
.Lsel_pa2_g0:
	v_exp_f32_e32 v244, v88
	v_exp_f32_e32 v245, v89
	v_exp_f32_e32 v246, v90
	v_exp_f32_e32 v247, v91
	s_waitcnt lgkmcnt(0)
	v_cvt_pk_fp8_f32 v84, v240, v241
	v_cvt_pk_fp8_f32 v85, v244, v245
	v_cvt_pk_fp8_f32 v84, v242, v243 op_sel:[0,0,1]
	v_cvt_pk_fp8_f32 v85, v246, v247 op_sel:[0,0,1]
	v_exp_f32_e32 v248, v92
	v_exp_f32_e32 v249, v93
	v_mfma_f32_16x16x32_fp8_fp8 v[80:83], v[134:135], v[84:85], v[80:83]
	v_exp_f32_e32 v250, v94
	v_mfma_f32_16x16x32_fp8_fp8 v[76:79], v[138:139], v[84:85], v[76:79]
	v_exp_f32_e32 v251, v95
	v_mfma_f32_16x16x32_fp8_fp8 v[72:75], v[142:143], v[84:85], v[72:75]
	v_exp_f32_e32 v252, v96
	v_mfma_f32_16x16x32_fp8_fp8 v[68:71], v[146:147], v[84:85], v[68:71]
	v_exp_f32_e32 v253, v97
	v_mfma_f32_16x16x32_fp8_fp8 v[64:67], v[118:119], v[84:85], v[64:67]
	v_exp_f32_e32 v254, v98
	v_mfma_f32_16x16x32_fp8_fp8 v[60:63], v[122:123], v[84:85], v[60:63]
	v_exp_f32_e32 v255, v99
	v_mfma_f32_16x16x32_fp8_fp8 v[56:59], v[126:127], v[84:85], v[56:59]
	v_mfma_f32_16x16x32_fp8_fp8 v[52:55], v[130:131], v[84:85], v[52:55]
	v_cvt_pk_fp8_f32 v86, v248, v249
	v_cvt_pk_fp8_f32 v87, v252, v253
	v_cvt_pk_fp8_f32 v86, v250, v251 op_sel:[0,0,1]
	v_cvt_pk_fp8_f32 v87, v254, v255 op_sel:[0,0,1]
	v_add_f32_e32 v240, v240, v241
	v_add_f32_e32 v242, v242, v243
	v_mfma_f32_16x16x32_fp8_fp8 v[80:83], v[136:137], v[86:87], v[80:83]
	v_add_f32_e32 v244, v244, v245
	v_add_f32_e32 v246, v246, v247
	v_mfma_f32_16x16x32_fp8_fp8 v[76:79], v[140:141], v[86:87], v[76:79]
	v_add_f32_e32 v248, v248, v249
	v_add_f32_e32 v250, v250, v251
	v_mfma_f32_16x16x32_fp8_fp8 v[72:75], v[144:145], v[86:87], v[72:75]
	v_add_f32_e32 v252, v252, v253
	v_add_f32_e32 v254, v254, v255
	v_mfma_f32_16x16x32_fp8_fp8 v[68:71], v[148:149], v[86:87], v[68:71]
	v_add_f32_e32 v240, v240, v242
	v_add_f32_e32 v244, v244, v246
	v_mfma_f32_16x16x32_fp8_fp8 v[64:67], v[120:121], v[86:87], v[64:67]
	v_add_f32_e32 v248, v248, v250
	v_add_f32_e32 v252, v252, v254
	v_mfma_f32_16x16x32_fp8_fp8 v[60:63], v[124:125], v[86:87], v[60:63]
	v_add_f32_e32 v240, v240, v244
	v_add_f32_e32 v248, v248, v252
	v_mfma_f32_16x16x32_fp8_fp8 v[56:59], v[128:129], v[86:87], v[56:59]
	v_add_f32_e32 v240, v240, v248
	v_add_f32_e32 v183, v183, v240
	v_mfma_f32_16x16x32_fp8_fp8 v[52:55], v[132:133], v[86:87], v[52:55]

; __device__ __forceinline__ unsigned pk4_fp8(float a, float b, float c, float d) { unsigned w = 0u; w = __builtin_amdgcn_cvt_pk_fp8_f32(a, b, w, false); w = __builtin_amdgcn_cvt_pk_fp8_f32(c, d, w, true); return w; }
; __device__ __forceinline__ float xmax16(float v) { float a = v, b = v; PL_SWAP16(a, b); return fmaxf(a, b); }
; __device__ __forceinline__ float xmax32(float v) { float a = v, b = v; PL_SWAP32(a, b); return fmaxf(a, b); }
; #define LGKM_W(n) asm volatile("s_waitcnt lgkmcnt(" #n ")" ::: "memory"); SBAR()
; #define PV8_MM(dt) do { g.o[dt] = __builtin_amdgcn_mfma_f32_16x16x32_fp8_fp8(f.a[dt][0], b0, g.o[dt], 0, 0, 0); g.o[dt] = __builtin_amdgcn_mfma_f32_16x16x32_fp8_fp8(f.a[dt][1], b1, g.o[dt], 0, 0, 0); } while (0)
; template <class G> __device__ __forceinline__ void pv8_mm(G& g, const f32x4 (&s)[4], const VT8Frag& f) {
;     ...
;     unsigned pa[4];
; #pragma unroll
;     for (int T_ = 0; T_ < 4; ++T_) pa[T_] = pk4_fp8(s[T_][0], s[T_][1], s[T_][2], s[T_][3]);
;     const long b0 = (long)(((unsigned long long)pa[1] << 32) | pa[0]), b1 = (long)(((unsigned long long)pa[3] << 32) | pa[2]);
;     LGKM_W(14); PV8_MM(0); LGKM_W(12); PV8_MM(1); LGKM_W(10); PV8_MM(2); LGKM_W(8); PV8_MM(3);
;     LGKM_W(6); PV8_MM(4); LGKM_W(4); PV8_MM(5); LGKM_W(2); PV8_MM(6); LGKM_W(0); PV8_MM(7);
; template <class G> __device__ __forceinline__ void online_sm8(f32x4 (&s)[4], G& g, const float ref) {
;     float mx = s[0][0];
; #pragma unroll
;     for (int T_ = 0; T_ < 4; ++T_)
; #pragma unroll
;         for (int i = 0; i < 4; ++i) mx = fmaxf(mx, s[T_][i]);
;     const float t = mx + (ref - 5.f);
;     if (!__all(t <= g.m + SM_THR8)) {
;         const float mr = xmax32(xmax16(t));
;         const float mn = fmaxf(g.m, mr); const float al = __builtin_amdgcn_exp2f(g.m - mn); g.m = mn; g.l *= al;
; #pragma unroll
;         for (int dt = 0; dt < 8; ++dt) g.o[dt] = g.o[dt] * al;
;         const float d = ref - mn;
; #pragma unroll
;         for (int T_ = 0; T_ < 4; ++T_)
; #pragma unroll
;             for (int i = 0; i < 4; ++i) s[T_][i] += d;
;     }
;     float ps = 0.f;
; #pragma unroll
;     for (int T_ = 0; T_ < 4; ++T_)
; #pragma unroll
;         for (int i = 0; i < 4; ++i) { s[T_][i] = __builtin_amdgcn_exp2f(s[T_][i]); ps += s[T_][i]; }
;     g.l += ps;
.LBB0_1812:
	v_max_f32_e32 v114, v84, v85
	v_max3_f32 v114, v114, v86, v87
	v_max3_f32 v114, v114, v88, v89
	v_max3_f32 v114, v114, v90, v91
	v_max3_f32 v114, v114, v92, v93
	v_max3_f32 v114, v114, v94, v95
	v_max3_f32 v114, v114, v96, v97
	v_max3_f32 v114, v114, v98, v99
	v_cmp_nle_f32_e32 vcc, v114, v227
	v_exp_f32_e32 v240, v84
	v_exp_f32_e32 v241, v85
	v_exp_f32_e32 v242, v86
	v_exp_f32_e32 v243, v87
	s_cbranch_vccnz .Lsel_resc_g1
.Lsel_pa2_g1:
	v_exp_f32_e32 v244, v88
	v_exp_f32_e32 v245, v89
	v_exp_f32_e32 v246, v90
	v_exp_f32_e32 v247, v91
	s_waitcnt lgkmcnt(0)
	v_cvt_pk_fp8_f32 v84, v240, v241
	v_cvt_pk_fp8_f32 v85, v244, v245
	v_cvt_pk_fp8_f32 v84, v242, v243 op_sel:[0,0,1]
	v_cvt_pk_fp8_f32 v85, v246, v247 op_sel:[0,0,1]
	v_exp_f32_e32 v248, v92
	v_exp_f32_e32 v249, v93
	v_mfma_f32_16x16x32_fp8_fp8 v[48:51], v[134:135], v[84:85], v[48:51]
	v_exp_f32_e32 v250, v94
	v_mfma_f32_16x16x32_fp8_fp8 v[44:47], v[138:139], v[84:85], v[44:47]
	v_exp_f32_e32 v251, v95
	v_mfma_f32_16x16x32_fp8_fp8 v[40:43], v[142:143], v[84:85], v[40:43]
	v_exp_f32_e32 v252, v96
	v_mfma_f32_16x16x32_fp8_fp8 v[36:39], v[146:147], v[84:85], v[36:39]
	v_exp_f32_e32 v253, v97
	v_mfma_f32_16x16x32_fp8_fp8 v[32:35], v[118:119], v[84:85], v[32:35]
	v_exp_f32_e32 v254, v98
	v_mfma_f32_16x16x32_fp8_fp8 v[28:31], v[122:123], v[84:85], v[28:31]
	v_exp_f32_e32 v255, v99
	v_mfma_f32_16x16x32_fp8_fp8 v[24:27], v[126:127], v[84:85], v[24:27]
	v_mfma_f32_16x16x32_fp8_fp8 v[20:23], v[130:131], v[84:85], v[20:23]
	v_cvt_pk_fp8_f32 v86, v248, v249
	v_cvt_pk_fp8_f32 v87, v252, v253
	v_cvt_pk_fp8_f32 v86, v250, v251 op_sel:[0,0,1]
	v_cvt_pk_fp8_f32 v87, v254, v255 op_sel:[0,0,1]
	v_add_f32_e32 v240, v240, v241
	v_add_f32_e32 v242, v242, v243
	v_mfma_f32_16x16x32_fp8_fp8 v[48:51], v[136:137], v[86:87], v[48:51]
	v_add_f32_e32 v244, v244, v245
	v_add_f32_e32 v246, v246, v247
	v_mfma_f32_16x16x32_fp8_fp8 v[44:47], v[140:141], v[86:87], v[44:47]
	v_add_f32_e32 v248, v248, v249
	v_add_f32_e32 v250, v250, v251
	v_mfma_f32_16x16x32_fp8_fp8 v[40:43], v[144:145], v[86:87], v[40:43]
	v_add_f32_e32 v252, v252, v253
	v_add_f32_e32 v254, v254, v255
	v_mfma_f32_16x16x32_fp8_fp8 v[36:39], v[148:149], v[86:87], v[36:39]
	v_add_f32_e32 v240, v240, v242
	v_add_f32_e32 v244, v244, v246
	v_mfma_f32_16x16x32_fp8_fp8 v[32:35], v[120:121], v[86:87], v[32:35]
	v_add_f32_e32 v248, v248, v250
	v_add_f32_e32 v252, v252, v254
	v_mfma_f32_16x16x32_fp8_fp8 v[28:31], v[124:125], v[86:87], v[28:31]
	v_add_f32_e32 v240, v240, v244
	v_add_f32_e32 v248, v248, v252
	v_mfma_f32_16x16x32_fp8_fp8 v[24:27], v[128:129], v[86:87], v[24:27]
	v_add_f32_e32 v240, v240, v248
	v_add_f32_e32 v182, v182, v240
	v_mfma_f32_16x16x32_fp8_fp8 v[20:23], v[132:133], v[86:87], v[20:23]
	s_branch .LBB0_1798
